# slim + cross-lane shuffles as v_permlane16/32_swap instead of ds_bpermute round trips: attention softmax row-max/row-sum (3 phases) and P1 q/k-norm sum-of-squares reduction (32 serialized hops per q/k
# speedup vs baseline: 1.0025x; 1.0025x over previous
;     DI void operator()(const f32x4 (&acc)[2][2][4][2], const Unit& u, int wr, int wc, int fr, int fq, const LAS unsigned char* st) const {
;     ...
;                 for (int bj = 0; bj < 2; ++bj) { const f32x4 v0 = acc[ai][bj][m][0], v1 = acc[ai][bj][m][1];
;                     float ss = (v0[0] * v0[0] + v0[1] * v0[1]) + (v0[2] * v0[2] + v0[3] * v0[3]) + (v1[0] * v1[0] + v1[1] * v1[1]) + (v1[2] * v1[2] + v1[3] * v1[3]);
;                     ss += __shfl_xor(ss, 16); ss += __shfl_xor(ss, 32);
;                     if (fq == 0) P[((ai * HALF + wr * 64 + m * 16 + fr) * 2 + bj) * 4 + wc] = ss; }
.LBB0_125:
	v_mul_f32_e32 v158, v127, v127
	v_mul_f32_e32 v159, v129, v129
	v_fmac_f32_e32 v158, v126, v126
	v_fmac_f32_e32 v159, v128, v128
	v_and_b32_e32 v157, 64, v236
	v_add_f32_e32 v158, v158, v159
	v_mul_f32_e32 v159, v123, v123
	v_xor_b32_e32 v155, 16, v236
	v_add_u32_e32 v157, 64, v157
	v_fmac_f32_e32 v159, v122, v122
	v_cmp_lt_i32_e32 vcc, v155, v157
	v_add_f32_e32 v158, v159, v158
	v_mul_f32_e32 v159, v125, v125
	v_cndmask_b32_e32 v155, v236, v155, vcc
	v_fmac_f32_e32 v159, v124, v124
	v_lshlrev_b32_e32 v155, 2, v155
	v_add_f32_e32 v158, v159, v158
	v_mov_b32_e32 v159, v158
	s_nop 1
	v_permlane16_swap_b32_e32 v159, v158
	v_xor_b32_e32 v160, 32, v236
	v_cmp_lt_i32_e32 vcc, v160, v157
	v_add_u32_e32 v195, s77, v154
	s_nop 0
	v_cndmask_b32_e32 v157, v236, v160, vcc
	v_lshlrev_b32_e32 v243, 2, v157
	s_waitcnt lgkmcnt(0)
	v_add_f32_e32 v157, v158, v159
	v_mov_b32_e32 v158, v157
	s_nop 1
	v_permlane32_swap_b32_e32 v158, v157
	v_cmp_gt_u32_e32 vcc, 16, v156
	v_lshl_add_u32 v156, s59, 2, v195
	s_and_saveexec_b64 s[0:1], vcc
	s_cbranch_execz .LBB0_127
	s_waitcnt lgkmcnt(0)
	v_add_f32_e32 v157, v157, v158
	ds_write_b32 v156, v157
.LBB0_127:
	s_or_b64 exec, exec, s[0:1]
	v_mul_f32_e32 v157, v115, v115
	s_waitcnt lgkmcnt(0)
	v_mul_f32_e32 v158, v117, v117
	v_fmac_f32_e32 v157, v114, v114
	v_fmac_f32_e32 v158, v116, v116
	v_add_f32_e32 v157, v157, v158
	v_mul_f32_e32 v158, v107, v107
	v_fmac_f32_e32 v158, v106, v106
	v_add_f32_e32 v157, v158, v157
	v_mul_f32_e32 v158, v109, v109
	v_fmac_f32_e32 v158, v108, v108
	v_add_f32_e32 v157, v158, v157
	v_mov_b32_e32 v158, v157
	s_nop 1
	v_permlane16_swap_b32_e32 v158, v157
	s_waitcnt lgkmcnt(0)
	v_add_f32_e32 v157, v157, v158
	v_mov_b32_e32 v158, v157
	s_nop 1
	v_permlane32_swap_b32_e32 v158, v157
	s_and_saveexec_b64 s[0:1], vcc
	s_cbranch_execz .LBB0_129
	s_waitcnt lgkmcnt(0)
	v_add_f32_e32 v157, v157, v158
	ds_write_b32 v156, v157 offset:16
.LBB0_129:
	s_or_b64 exec, exec, s[0:1]
	v_mul_f32_e32 v156, v119, v119
	v_mul_f32_e32 v157, v121, v121
	v_fmac_f32_e32 v156, v118, v118
	v_fmac_f32_e32 v157, v120, v120
	v_add_f32_e32 v156, v156, v157
	v_mul_f32_e32 v157, v111, v111
	v_fmac_f32_e32 v157, v110, v110
	v_add_f32_e32 v156, v157, v156
	v_mul_f32_e32 v157, v113, v113
	v_fmac_f32_e32 v157, v112, v112
	v_add_f32_e32 v156, v157, v156
	v_mov_b32_e32 v157, v156
	s_nop 1
	v_permlane16_swap_b32_e32 v157, v156
	s_waitcnt lgkmcnt(0)
	v_add_f32_e32 v157, v156, v157
	v_mov_b32_e32 v158, v157
	s_nop 1
	v_permlane32_swap_b32_e32 v158, v157
	v_add_u32_e32 v156, s66, v154
	s_and_saveexec_b64 s[0:1], vcc
	s_cbranch_execz .LBB0_131
	s_waitcnt lgkmcnt(0)
	v_add_f32_e32 v157, v157, v158
	ds_write_b32 v156, v157
.LBB0_131:
	s_or_b64 exec, exec, s[0:1]
	v_mul_f32_e32 v157, v99, v99
	s_waitcnt lgkmcnt(0)
	v_mul_f32_e32 v158, v101, v101
	v_fmac_f32_e32 v157, v98, v98
	v_fmac_f32_e32 v158, v100, v100
	v_add_f32_e32 v157, v157, v158
	v_mul_f32_e32 v158, v91, v91
	v_fmac_f32_e32 v158, v90, v90
	v_add_f32_e32 v157, v158, v157
	v_mul_f32_e32 v158, v93, v93
	v_fmac_f32_e32 v158, v92, v92
	v_add_f32_e32 v157, v158, v157
	v_mov_b32_e32 v158, v157
	s_nop 1
	v_permlane16_swap_b32_e32 v158, v157
	s_waitcnt lgkmcnt(0)
	v_add_f32_e32 v157, v157, v158
	v_mov_b32_e32 v158, v157
	s_nop 1
	v_permlane32_swap_b32_e32 v158, v157
	s_and_saveexec_b64 s[0:1], vcc
	s_cbranch_execz .LBB0_133
	s_waitcnt lgkmcnt(0)
	v_add_f32_e32 v157, v157, v158
	ds_write_b32 v156, v157 offset:16
.LBB0_133:
	s_or_b64 exec, exec, s[0:1]
	v_mul_f32_e32 v156, v103, v103
	v_mul_f32_e32 v157, v105, v105
	v_fmac_f32_e32 v156, v102, v102
	v_fmac_f32_e32 v157, v104, v104
	v_add_f32_e32 v156, v156, v157
	v_mul_f32_e32 v157, v95, v95
	v_fmac_f32_e32 v157, v94, v94
	v_add_f32_e32 v156, v157, v156
	v_mul_f32_e32 v157, v97, v97
	v_fmac_f32_e32 v157, v96, v96
	v_add_f32_e32 v156, v157, v156
	v_mov_b32_e32 v157, v156
	s_nop 1
	v_permlane16_swap_b32_e32 v157, v156
	s_waitcnt lgkmcnt(0)
	v_add_f32_e32 v157, v156, v157
	v_mov_b32_e32 v158, v157
	s_nop 1
	v_permlane32_swap_b32_e32 v158, v157
	v_add_u32_e32 v156, s67, v154
	s_and_saveexec_b64 s[0:1], vcc
	s_cbranch_execz .LBB0_135
	s_waitcnt lgkmcnt(0)
	v_add_f32_e32 v157, v157, v158
	ds_write_b32 v156, v157
.LBB0_135:
	s_or_b64 exec, exec, s[0:1]
	v_mul_f32_e32 v157, v83, v83
	s_waitcnt lgkmcnt(0)
	v_mul_f32_e32 v158, v85, v85
	v_fmac_f32_e32 v157, v82, v82
	v_fmac_f32_e32 v158, v84, v84
	v_add_f32_e32 v157, v157, v158
	v_mul_f32_e32 v158, v75, v75
	v_fmac_f32_e32 v158, v74, v74
	v_add_f32_e32 v157, v158, v157
	v_mul_f32_e32 v158, v77, v77
	v_fmac_f32_e32 v158, v76, v76
	v_add_f32_e32 v157, v158, v157
	v_mov_b32_e32 v158, v157
	s_nop 1
	v_permlane16_swap_b32_e32 v158, v157
	s_waitcnt lgkmcnt(0)
	v_add_f32_e32 v157, v157, v158
	v_mov_b32_e32 v158, v157
	s_nop 1
	v_permlane32_swap_b32_e32 v158, v157
	s_and_saveexec_b64 s[0:1], vcc
	s_cbranch_execz .LBB0_137
	s_waitcnt lgkmcnt(0)
	v_add_f32_e32 v157, v157, v158
	ds_write_b32 v156, v157 offset:16
.LBB0_137:
	s_or_b64 exec, exec, s[0:1]
	v_mul_f32_e32 v156, v87, v87
	v_mul_f32_e32 v157, v89, v89
	v_fmac_f32_e32 v156, v86, v86
	v_fmac_f32_e32 v157, v88, v88
	v_add_f32_e32 v156, v156, v157
	v_mul_f32_e32 v157, v79, v79
	v_fmac_f32_e32 v157, v78, v78
	v_add_f32_e32 v156, v157, v156
	v_mul_f32_e32 v157, v81, v81
	v_fmac_f32_e32 v157, v80, v80
	v_add_f32_e32 v156, v157, v156
	v_mov_b32_e32 v157, v156
	s_nop 1
	v_permlane16_swap_b32_e32 v157, v156
	s_waitcnt lgkmcnt(0)
	v_add_f32_e32 v157, v156, v157
	v_mov_b32_e32 v158, v157
	s_nop 1
	v_permlane32_swap_b32_e32 v158, v157
	v_add_u32_e32 v156, s68, v154
	s_and_saveexec_b64 s[0:1], vcc
	s_cbranch_execz .LBB0_139
	s_waitcnt lgkmcnt(0)
	v_add_f32_e32 v157, v157, v158
	ds_write_b32 v156, v157
;     DI void operator()(const f32x4 (&acc)[2][2][4][2], const Unit& u, int wr, int wc, int fr, int fq, const LAS unsigned char* st) const {
;     ...
;                 for (int bj = 0; bj < 2; ++bj) { const f32x4 v0 = acc[ai][bj][m][0], v1 = acc[ai][bj][m][1];
;                     float ss = (v0[0] * v0[0] + v0[1] * v0[1]) + (v0[2] * v0[2] + v0[3] * v0[3]) + (v1[0] * v1[0] + v1[1] * v1[1]) + (v1[2] * v1[2] + v1[3] * v1[3]);
;                     ss += __shfl_xor(ss, 16); ss += __shfl_xor(ss, 32);
;                     if (fq == 0) P[((ai * HALF + wr * 64 + m * 16 + fr) * 2 + bj) * 4 + wc] = ss; }
.LBB0_139:
	s_or_b64 exec, exec, s[0:1]
	v_mul_f32_e32 v157, v71, v71
	s_waitcnt lgkmcnt(0)
	v_mul_f32_e32 v158, v73, v73
	v_fmac_f32_e32 v157, v70, v70
	v_fmac_f32_e32 v158, v72, v72
	v_add_f32_e32 v157, v157, v158
	v_mul_f32_e32 v158, v67, v67
	v_fmac_f32_e32 v158, v66, v66
	v_add_f32_e32 v157, v158, v157
	v_mul_f32_e32 v158, v69, v69
	v_fmac_f32_e32 v158, v68, v68
	v_add_f32_e32 v157, v158, v157
	v_mov_b32_e32 v158, v157
	s_nop 1
	v_permlane16_swap_b32_e32 v158, v157
	s_waitcnt lgkmcnt(0)
	v_add_f32_e32 v157, v157, v158
	v_mov_b32_e32 v158, v157
	s_nop 1
	v_permlane32_swap_b32_e32 v158, v157
	s_and_saveexec_b64 s[0:1], vcc
	s_cbranch_execz .LBB0_141
	s_waitcnt lgkmcnt(0)
	v_add_f32_e32 v157, v157, v158
	ds_write_b32 v156, v157 offset:16
.LBB0_141:
	s_or_b64 exec, exec, s[0:1]
	v_mul_f32_e32 v156, v63, v63
	v_mul_f32_e32 v157, v65, v65
	v_fmac_f32_e32 v156, v62, v62
	v_fmac_f32_e32 v157, v64, v64
	v_add_f32_e32 v156, v156, v157
	v_mul_f32_e32 v157, v59, v59
	v_fmac_f32_e32 v157, v58, v58
	v_add_f32_e32 v156, v157, v156
	v_mul_f32_e32 v157, v61, v61
	v_fmac_f32_e32 v157, v60, v60
	v_add_f32_e32 v156, v157, v156
	v_mov_b32_e32 v157, v156
	s_nop 1
	v_permlane16_swap_b32_e32 v157, v156
	s_waitcnt lgkmcnt(0)
	v_add_f32_e32 v157, v156, v157
	v_mov_b32_e32 v158, v157
	s_nop 1
	v_permlane32_swap_b32_e32 v158, v157
	v_add_u32_e32 v156, s69, v154
	s_and_saveexec_b64 s[0:1], vcc
	s_cbranch_execz .LBB0_143
	s_waitcnt lgkmcnt(0)
	v_add_f32_e32 v157, v157, v158
	ds_write_b32 v156, v157
.LBB0_143:
	s_or_b64 exec, exec, s[0:1]
	v_mul_f32_e32 v157, v51, v51
	s_waitcnt lgkmcnt(0)
	v_mul_f32_e32 v158, v53, v53
	v_fmac_f32_e32 v157, v50, v50
	v_fmac_f32_e32 v158, v52, v52
	v_add_f32_e32 v157, v157, v158
	v_mul_f32_e32 v158, v43, v43
	v_fmac_f32_e32 v158, v42, v42
	v_add_f32_e32 v157, v158, v157
	v_mul_f32_e32 v158, v45, v45
	v_fmac_f32_e32 v158, v44, v44
	v_add_f32_e32 v157, v158, v157
	v_mov_b32_e32 v158, v157
	s_nop 1
	v_permlane16_swap_b32_e32 v158, v157
	s_waitcnt lgkmcnt(0)
	v_add_f32_e32 v157, v157, v158
	v_mov_b32_e32 v158, v157
	s_nop 1
	v_permlane32_swap_b32_e32 v158, v157
	s_and_saveexec_b64 s[0:1], vcc
	s_cbranch_execz .LBB0_145
	s_waitcnt lgkmcnt(0)
	v_add_f32_e32 v157, v157, v158
	ds_write_b32 v156, v157 offset:16
.LBB0_145:
	s_or_b64 exec, exec, s[0:1]
	v_mul_f32_e32 v156, v55, v55
	v_mul_f32_e32 v157, v57, v57
	v_fmac_f32_e32 v156, v54, v54
	v_fmac_f32_e32 v157, v56, v56
	v_add_f32_e32 v156, v156, v157
	v_mul_f32_e32 v157, v47, v47
	v_fmac_f32_e32 v157, v46, v46
	v_add_f32_e32 v156, v157, v156
	v_mul_f32_e32 v157, v49, v49
	v_fmac_f32_e32 v157, v48, v48
	v_add_f32_e32 v156, v157, v156
	v_mov_b32_e32 v157, v156
	s_nop 1
	v_permlane16_swap_b32_e32 v157, v156
	s_waitcnt lgkmcnt(0)
	v_add_f32_e32 v157, v156, v157
	v_mov_b32_e32 v158, v157
	s_nop 1
	v_permlane32_swap_b32_e32 v158, v157
	v_add_u32_e32 v156, s70, v154
	s_and_saveexec_b64 s[0:1], vcc
	s_cbranch_execz .LBB0_147
	s_waitcnt lgkmcnt(0)
	v_add_f32_e32 v157, v157, v158
	ds_write_b32 v156, v157
.LBB0_147:
	s_or_b64 exec, exec, s[0:1]
	v_mul_f32_e32 v157, v35, v35
	s_waitcnt lgkmcnt(0)
	v_mul_f32_e32 v158, v37, v37
	v_fmac_f32_e32 v157, v34, v34
	v_fmac_f32_e32 v158, v36, v36
	v_add_f32_e32 v157, v157, v158
	v_mul_f32_e32 v158, v27, v27
	v_fmac_f32_e32 v158, v26, v26
	v_add_f32_e32 v157, v158, v157
	v_mul_f32_e32 v158, v29, v29
	v_fmac_f32_e32 v158, v28, v28
	v_add_f32_e32 v157, v158, v157
	v_mov_b32_e32 v158, v157
	s_nop 1
	v_permlane16_swap_b32_e32 v158, v157
	s_waitcnt lgkmcnt(0)
	v_add_f32_e32 v157, v157, v158
	v_mov_b32_e32 v158, v157
	s_nop 1
	v_permlane32_swap_b32_e32 v158, v157
	s_and_saveexec_b64 s[0:1], vcc
	s_cbranch_execz .LBB0_149
	s_waitcnt lgkmcnt(0)
	v_add_f32_e32 v157, v157, v158
	ds_write_b32 v156, v157 offset:16
.LBB0_149:
	s_or_b64 exec, exec, s[0:1]
	v_mul_f32_e32 v156, v39, v39
	v_mul_f32_e32 v157, v41, v41
	v_fmac_f32_e32 v156, v38, v38
	v_fmac_f32_e32 v157, v40, v40
	v_add_f32_e32 v156, v156, v157
	v_mul_f32_e32 v157, v31, v31
	v_fmac_f32_e32 v157, v30, v30
	v_add_f32_e32 v156, v157, v156
	v_mul_f32_e32 v157, v33, v33
	v_fmac_f32_e32 v157, v32, v32
	v_add_f32_e32 v156, v157, v156
	v_mov_b32_e32 v157, v156
	s_nop 1
	v_permlane16_swap_b32_e32 v157, v156
	s_waitcnt lgkmcnt(0)
	v_add_f32_e32 v157, v156, v157
	v_mov_b32_e32 v158, v157
	s_nop 1
	v_permlane32_swap_b32_e32 v158, v157
	v_add_u32_e32 v156, s71, v154
	s_and_saveexec_b64 s[0:1], vcc
	s_cbranch_execz .LBB0_151
	s_waitcnt lgkmcnt(0)
	v_add_f32_e32 v157, v157, v158
	ds_write_b32 v156, v157
.LBB0_151:
	s_or_b64 exec, exec, s[0:1]
	v_mul_f32_e32 v157, v19, v19
	s_waitcnt lgkmcnt(0)
	v_mul_f32_e32 v158, v21, v21
	v_fmac_f32_e32 v157, v18, v18
	v_fmac_f32_e32 v158, v20, v20
	v_add_f32_e32 v157, v157, v158
	v_mul_f32_e32 v158, v11, v11
	v_fmac_f32_e32 v158, v10, v10
	v_add_f32_e32 v157, v158, v157
	v_mul_f32_e32 v158, v13, v13
	v_fmac_f32_e32 v158, v12, v12
	v_add_f32_e32 v157, v158, v157
	v_mov_b32_e32 v158, v157
	s_nop 1
	v_permlane16_swap_b32_e32 v158, v157
	s_waitcnt lgkmcnt(0)
	v_add_f32_e32 v157, v157, v158
	v_mov_b32_e32 v158, v157
	s_nop 1
	v_permlane32_swap_b32_e32 v158, v157
	s_and_saveexec_b64 s[0:1], vcc
	s_cbranch_execz .LBB0_153
	s_waitcnt lgkmcnt(0)
	v_add_f32_e32 v157, v157, v158
	ds_write_b32 v156, v157 offset:16
.LBB0_153:
	s_or_b64 exec, exec, s[0:1]
	v_mul_f32_e32 v156, v23, v23
	v_mul_f32_e32 v157, v25, v25
	v_fmac_f32_e32 v156, v22, v22
	v_fmac_f32_e32 v157, v24, v24
	v_add_f32_e32 v156, v156, v157
	v_mul_f32_e32 v157, v15, v15
	v_fmac_f32_e32 v157, v14, v14
	v_add_f32_e32 v156, v157, v156
	v_mul_f32_e32 v157, v17, v17
	v_fmac_f32_e32 v157, v16, v16
	v_add_f32_e32 v156, v157, v156
	v_mov_b32_e32 v157, v156
	s_nop 1
	v_permlane16_swap_b32_e32 v157, v156
	v_add_u32_e32 v154, s74, v154
	s_waitcnt lgkmcnt(0)
	v_add_f32_e32 v156, v156, v157
	v_mov_b32_e32 v157, v156
	s_nop 1
	v_permlane32_swap_b32_e32 v157, v156
	s_and_saveexec_b64 s[0:1], vcc
	s_cbranch_execz .LBB0_155
	s_waitcnt lgkmcnt(0)
	v_add_f32_e32 v156, v156, v157
	ds_write_b32 v154, v156
.LBB0_155:
	s_or_b64 exec, exec, s[0:1]
	v_mul_f32_e32 v156, v7, v7
	s_waitcnt lgkmcnt(0)
	v_mul_f32_e32 v157, v9, v9
	v_fmac_f32_e32 v156, v6, v6
	v_fmac_f32_e32 v157, v8, v8
	v_add_f32_e32 v156, v156, v157
	v_mul_f32_e32 v157, v3, v3
	v_fmac_f32_e32 v157, v2, v2
	v_add_f32_e32 v156, v157, v156
	v_mul_f32_e32 v157, v5, v5
	v_fmac_f32_e32 v157, v4, v4
	v_add_f32_e32 v156, v157, v156
	v_mov_b32_e32 v155, v156
	s_nop 1
	v_permlane16_swap_b32_e32 v155, v156
	s_waitcnt lgkmcnt(0)
	v_add_f32_e32 v155, v156, v155
	v_mov_b32_e32 v156, v155
	s_nop 1
	v_permlane32_swap_b32_e32 v156, v155
	s_and_saveexec_b64 s[0:1], vcc
	s_cbranch_execz .LBB0_157
	s_waitcnt lgkmcnt(0)
	v_add_f32_e32 v155, v155, v156
	ds_write_b32 v154, v155 offset:16

; template <int DIL, bool FIRST, bool LAST>
; DI void attn_phase(Frame& F) {
;     ...
;                     float mx = fmaxf(fmaxf(s[0], s[1]), s[2]);
; #pragma unroll
;                     for (int e = 3; e < 15; e += 2) mx = fmaxf(fmaxf(mx, s[e]), s[e + 1]);
;                     mx = fmaxf(mx, s[15]);
;                     mx = fmaxf(mx, __shfl_xor(mx, 32));
;                     if (__any(mx > m + 8.0f)) { const float mn = fmaxf(m, mx), alpha = __builtin_amdgcn_exp2f(m - mn); l *= alpha; m = mn;
; #pragma unroll
;                         for (int db = 0; db < 4; ++db)
; #pragma unroll
;                             for (int e = 0; e < 16; ++e) o[db][e] *= alpha; }
.LBB0_382:
	s_nop 1
	v_max_f32_e32 v2, v83, v83
	v_max_f32_e32 v16, v82, v82
	v_max_f32_e32 v2, v16, v2
	v_max3_f32 v2, v2, v84, v85
	v_max3_f32 v2, v2, v86, v87
	v_max3_f32 v2, v2, v88, v89
	v_max3_f32 v2, v2, v90, v91
	v_max3_f32 v2, v2, v92, v93
	v_max3_f32 v2, v2, v94, v95
	v_and_b32_e32 v17, 64, v198
	v_max3_f32 v16, v2, v96, v97
	v_xor_b32_e32 v2, 32, v198
	v_add_u32_e32 v17, 64, v17
	v_cmp_lt_i32_e32 vcc, v2, v17
	s_nop 1
	v_cndmask_b32_e32 v2, v198, v2, vcc
	v_lshlrev_b32_e32 v2, 2, v2
	v_mov_b32_e32 v17, v16
	s_nop 1
	v_permlane32_swap_b32_e32 v17, v16
	s_waitcnt lgkmcnt(0)
	v_max_f32_e32 v17, v17, v17
	v_max_f32_e32 v16, v16, v17
	v_add_f32_e32 v17, 0x41000000, v158
	v_cmp_gt_f32_e32 vcc, v16, v17
	s_cbranch_vccz .LBB0_384
	v_max_f32_e32 v16, v16, v16
	v_max_f32_e32 v17, v158, v158
	v_max_f32_e32 v17, v17, v16
	v_sub_f32_e32 v16, v158, v17
	v_exp_f32_e32 v16, v16
	v_mov_b32_e32 v158, v17
	v_pk_mul_f32 v[32:33], v[32:33], v[16:17] op_sel_hi:[1,0]
	v_pk_mul_f32 v[30:31], v[30:31], v[16:17] op_sel_hi:[1,0]
	v_pk_mul_f32 v[28:29], v[28:29], v[16:17] op_sel_hi:[1,0]
	v_pk_mul_f32 v[26:27], v[26:27], v[16:17] op_sel_hi:[1,0]
	v_pk_mul_f32 v[24:25], v[24:25], v[16:17] op_sel_hi:[1,0]
	v_pk_mul_f32 v[22:23], v[22:23], v[16:17] op_sel_hi:[1,0]
	v_pk_mul_f32 v[20:21], v[20:21], v[16:17] op_sel_hi:[1,0]
	v_pk_mul_f32 v[18:19], v[18:19], v[16:17] op_sel_hi:[1,0]
	v_pk_mul_f32 v[48:49], v[48:49], v[16:17] op_sel_hi:[1,0]
	v_pk_mul_f32 v[46:47], v[46:47], v[16:17] op_sel_hi:[1,0]
	v_pk_mul_f32 v[44:45], v[44:45], v[16:17] op_sel_hi:[1,0]
	v_pk_mul_f32 v[42:43], v[42:43], v[16:17] op_sel_hi:[1,0]
	v_pk_mul_f32 v[40:41], v[40:41], v[16:17] op_sel_hi:[1,0]
	v_pk_mul_f32 v[38:39], v[38:39], v[16:17] op_sel_hi:[1,0]
	v_pk_mul_f32 v[36:37], v[36:37], v[16:17] op_sel_hi:[1,0]
	v_pk_mul_f32 v[34:35], v[34:35], v[16:17] op_sel_hi:[1,0]
	v_pk_mul_f32 v[64:65], v[64:65], v[16:17] op_sel_hi:[1,0]
	v_pk_mul_f32 v[62:63], v[62:63], v[16:17] op_sel_hi:[1,0]
	v_pk_mul_f32 v[60:61], v[60:61], v[16:17] op_sel_hi:[1,0]
	v_pk_mul_f32 v[58:59], v[58:59], v[16:17] op_sel_hi:[1,0]
	v_pk_mul_f32 v[56:57], v[56:57], v[16:17] op_sel_hi:[1,0]
	v_pk_mul_f32 v[54:55], v[54:55], v[16:17] op_sel_hi:[1,0]
	v_pk_mul_f32 v[52:53], v[52:53], v[16:17] op_sel_hi:[1,0]
	v_pk_mul_f32 v[50:51], v[50:51], v[16:17] op_sel_hi:[1,0]
	v_pk_mul_f32 v[80:81], v[80:81], v[16:17] op_sel_hi:[1,0]
	v_pk_mul_f32 v[78:79], v[78:79], v[16:17] op_sel_hi:[1,0]
	v_pk_mul_f32 v[76:77], v[76:77], v[16:17] op_sel_hi:[1,0]
	v_pk_mul_f32 v[74:75], v[74:75], v[16:17] op_sel_hi:[1,0]
	v_pk_mul_f32 v[72:73], v[72:73], v[16:17] op_sel_hi:[1,0]
	v_pk_mul_f32 v[70:71], v[70:71], v[16:17] op_sel_hi:[1,0]
	v_pk_mul_f32 v[68:69], v[68:69], v[16:17] op_sel_hi:[1,0]
	v_pk_mul_f32 v[66:67], v[66:67], v[16:17] op_sel_hi:[1,0]
	v_mul_f32_e32 v159, v159, v16
; DI unsigned cvtpk(float lo, float hi) { f32x2 v = {lo, hi}; bf16x2_t b = __builtin_convertvector(v, bf16x2_t); return __builtin_bit_cast(unsigned, b); }
; DI f32x16 mfma32(bf16x8 a, bf16x8 b, f32x16 c) { return __builtin_amdgcn_mfma_f32_32x32x16_bf16(a, b, c, 0, 0, 0); }
; template <int DIL, bool FIRST, bool LAST>
; DI void attn_phase(Frame& F) {
;     ...
;                     float rs = 0.f;
; #pragma unroll
;                     for (int e = 0; e < 16; ++e) { s[e] = __builtin_amdgcn_exp2f(s[e] - m); rs += s[e]; }
;                     rs += __shfl_xor(rs, 32); l += rs;
;                     bf16x8 pb[2];
; #pragma unroll
;                     for (int s2 = 0; s2 < 2; ++s2) { u32x4 w; w.x = cvtpk(s[8 * s2], s[8 * s2 + 1]); w.y = cvtpk(s[8 * s2 + 2], s[8 * s2 + 3]); w.z = cvtpk(s[8 * s2 + 4], s[8 * s2 + 5]); w.w = cvtpk(s[8 * s2 + 6], s[8 * s2 + 7]);
;                         pb[s2] = __builtin_bit_cast(bf16x8, w); }
; #pragma unroll
;                     for (int s2 = 0; s2 < 2; ++s2) {
; #pragma unroll
;                         for (int db = 0; db < 4; ++db) o[db] = mfma32(va[s2][db], pb[s2], o[db]);
;                     }
;     ...
;                         } else {
;                             bf16* ostp = OST + hrow * 128 + 8 * h; float* mlp = ML + hrow * 2;
; #pragma unroll
;                             for (int db = 0; db < 4; ++db)
; #pragma unroll
;                                 for (int j2 = 0; j2 < 2; ++j2) { u32x2 w2[2];
; #pragma unroll
;                                     for (int q2 = 0; q2 < 2; ++q2) { const int g4 = 2 * j2 + q2; w2[q2].x = cvtpk(o[db][4 * g4], o[db][4 * g4 + 1]); w2[q2].y = cvtpk(o[db][4 * g4 + 2], o[db][4 * g4 + 3]); }
;                                     swap32(w2[0], w2[1]); u32x4 w; w.x = w2[0].x; w.y = w2[0].y; w.z = w2[1].x; w.w = w2[1].y;
;                                     *(u32x4*)(ostp + 32 * db + 16 * j2) = w; }
;                             if (h == 0) { f32x2 mlv; mlv[0] = m; mlv[1] = l; *(f32x2*)mlp = mlv; }
.LBB0_384:
	v_sub_f32_e32 v16, v82, v158
	v_exp_f32_e32 v16, v16
	v_sub_f32_e32 v82, v83, v158
	v_exp_f32_e32 v82, v82
	v_sub_f32_e32 v83, v84, v158
	v_exp_f32_e32 v83, v83
	v_sub_f32_e32 v84, v85, v158
	v_exp_f32_e32 v84, v84
	v_sub_f32_e32 v85, v86, v158
	v_add_f32_e32 v17, 0, v16
	v_exp_f32_e32 v85, v85
	v_sub_f32_e32 v86, v87, v158
	v_add_f32_e32 v17, v82, v17
	v_exp_f32_e32 v86, v86
	v_sub_f32_e32 v87, v88, v158
	v_sub_f32_e32 v88, v89, v158
	v_add_f32_e32 v17, v83, v17
	v_exp_f32_e32 v87, v87
	v_exp_f32_e32 v88, v88
	v_add_f32_e32 v17, v84, v17
	v_sub_f32_e32 v89, v90, v158
	v_add_f32_e32 v17, v85, v17
	v_exp_f32_e32 v89, v89
	v_sub_f32_e32 v90, v91, v158
	v_add_f32_e32 v17, v86, v17
	v_exp_f32_e32 v90, v90
	v_sub_f32_e32 v91, v92, v158
	v_add_f32_e32 v17, v87, v17
	v_exp_f32_e32 v91, v91
	v_sub_f32_e32 v92, v93, v158
	v_cvt_pk_bf16_f32 v82, v16, v82
	v_cvt_pk_bf16_f32 v83, v83, v84
	v_cvt_pk_bf16_f32 v84, v85, v86
	v_cvt_pk_bf16_f32 v85, v87, v88
	v_add_f32_e32 v17, v88, v17
	v_exp_f32_e32 v92, v92
	v_sub_f32_e32 v93, v94, v158
	v_mfma_f32_32x32x16_bf16 v[18:33], v[142:145], v[82:85], v[18:33]
	v_add_f32_e32 v17, v89, v17
	v_exp_f32_e32 v93, v93
	v_sub_f32_e32 v94, v95, v158
	v_add_f32_e32 v17, v90, v17
	v_exp_f32_e32 v94, v94
	v_sub_f32_e32 v95, v96, v158
	v_sub_f32_e32 v96, v97, v158
	v_mfma_f32_32x32x16_bf16 v[34:49], v[146:149], v[82:85], v[34:49]
	v_add_f32_e32 v17, v91, v17
	v_exp_f32_e32 v95, v95
	v_exp_f32_e32 v96, v96
	v_add_f32_e32 v17, v92, v17
	v_add_f32_e32 v17, v93, v17
	v_add_f32_e32 v17, v94, v17
	v_add_f32_e32 v17, v95, v17
	v_mfma_f32_32x32x16_bf16 v[50:65], v[138:141], v[82:85], v[50:65]
	v_cvt_pk_bf16_f32 v86, v89, v90
	v_cvt_pk_bf16_f32 v87, v91, v92
	v_cvt_pk_bf16_f32 v88, v93, v94
	v_cvt_pk_bf16_f32 v89, v95, v96
	v_add_f32_e32 v17, v96, v17
	v_mov_b32_e32 v2, v17
	s_nop 1
	v_permlane32_swap_b32_e32 v2, v17
	s_andn2_b64 vcc, exec, s[88:89]
	v_mfma_f32_32x32x16_bf16 v[66:81], v[134:137], v[82:85], v[66:81]
	s_waitcnt lgkmcnt(0)
	v_add_f32_e32 v2, v17, v2
	v_add_f32_e32 v159, v159, v2
	v_mfma_f32_32x32x16_bf16 v[18:33], v[130:133], v[86:89], v[18:33]
	v_mfma_f32_32x32x16_bf16 v[34:49], v[12:15], v[86:89], v[34:49]
	v_mfma_f32_32x32x16_bf16 v[50:65], v[8:11], v[86:89], v[50:65]
	v_mfma_f32_32x32x16_bf16 v[66:81], v[4:7], v[86:89], v[66:81]
	s_cbranch_vccnz .LBB0_366
	v_or_b32_e32 v4, s73, v1
	v_ashrrev_i32_e32 v5, 31, v4
	v_lshl_add_u64 v[4:5], s[84:85], 0, v[4:5]
	v_lshlrev_b64 v[6:7], 8, v[4:5]
	v_lshl_add_u64 v[10:11], v[150:151], 0, v[6:7]
	s_nop 2
	v_cvt_pk_bf16_f32 v6, v18, v19
	v_cvt_pk_bf16_f32 v7, v20, v21
	v_cvt_pk_bf16_f32 v8, v22, v23
	v_cvt_pk_bf16_f32 v9, v24, v25
	s_nop 0
	v_permlane32_swap_b32_e32 v6, v8
	v_permlane32_swap_b32_e32 v7, v9
	global_store_dwordx4 v[10:11], v[6:9], off
	s_nop 1
	v_cvt_pk_bf16_f32 v6, v26, v27
	v_cvt_pk_bf16_f32 v7, v28, v29
	v_cvt_pk_bf16_f32 v8, v30, v31
	v_cvt_pk_bf16_f32 v9, v32, v33
	s_nop 0
	v_permlane32_swap_b32_e32 v6, v8
	v_permlane32_swap_b32_e32 v7, v9
	global_store_dwordx4 v[10:11], v[6:9], off offset:32
	s_nop 1
	v_cvt_pk_bf16_f32 v6, v34, v35
	v_cvt_pk_bf16_f32 v7, v36, v37
	v_cvt_pk_bf16_f32 v8, v38, v39
	v_cvt_pk_bf16_f32 v9, v40, v41
	s_nop 0
	v_permlane32_swap_b32_e32 v6, v8
	v_permlane32_swap_b32_e32 v7, v9
	global_store_dwordx4 v[10:11], v[6:9], off offset:64
	s_nop 1
	v_cvt_pk_bf16_f32 v6, v42, v43
	v_cvt_pk_bf16_f32 v7, v44, v45
	v_cvt_pk_bf16_f32 v8, v46, v47
	v_cvt_pk_bf16_f32 v9, v48, v49
	s_nop 0
	v_permlane32_swap_b32_e32 v6, v8
	v_permlane32_swap_b32_e32 v7, v9
	global_store_dwordx4 v[10:11], v[6:9], off offset:96
	s_nop 1
	v_cvt_pk_bf16_f32 v6, v50, v51
	v_cvt_pk_bf16_f32 v7, v52, v53
	v_cvt_pk_bf16_f32 v8, v54, v55
	v_cvt_pk_bf16_f32 v9, v56, v57
	s_nop 0
	v_permlane32_swap_b32_e32 v6, v8
	v_permlane32_swap_b32_e32 v7, v9
	global_store_dwordx4 v[10:11], v[6:9], off offset:128
	s_nop 1
	v_cvt_pk_bf16_f32 v6, v58, v59
	v_cvt_pk_bf16_f32 v7, v60, v61
	v_cvt_pk_bf16_f32 v8, v62, v63
	v_cvt_pk_bf16_f32 v9, v64, v65
	s_nop 0
	v_permlane32_swap_b32_e32 v6, v8
	v_permlane32_swap_b32_e32 v7, v9
	global_store_dwordx4 v[10:11], v[6:9], off offset:160
	s_nop 1
	v_cvt_pk_bf16_f32 v6, v66, v67
	v_cvt_pk_bf16_f32 v7, v68, v69
	v_cvt_pk_bf16_f32 v8, v70, v71
	v_cvt_pk_bf16_f32 v9, v72, v73
	s_nop 0
	v_permlane32_swap_b32_e32 v6, v8
	v_permlane32_swap_b32_e32 v7, v9
	global_store_dwordx4 v[10:11], v[6:9], off offset:192
	s_nop 1
	v_cvt_pk_bf16_f32 v6, v74, v75
	v_cvt_pk_bf16_f32 v7, v76, v77
	v_cvt_pk_bf16_f32 v8, v78, v79
	v_cvt_pk_bf16_f32 v9, v80, v81
	s_nop 0
	v_permlane32_swap_b32_e32 v6, v8
	v_permlane32_swap_b32_e32 v7, v9
	global_store_dwordx4 v[10:11], v[6:9], off offset:224
	s_mov_b64 s[0:1], exec
	v_readlane_b32 s2, v254, 54
	v_readlane_b32 s3, v254, 55
	s_and_b64 s[2:3], s[0:1], s[2:3]
	s_mov_b64 exec, s[2:3]
	s_cbranch_execnz .LBB0_388
	s_or_b64 exec, exec, s[0:1]
	s_cmp_gt_i32 s76, 2
	s_mov_b64 s[0:1], -1
	s_cbranch_scc1 .LBB0_389

; template <int DIL, bool FIRST, bool LAST>
; DI void attn_phase(Frame& F) {
;     ...
;                     float mx = fmaxf(fmaxf(s[0], s[1]), s[2]);
; #pragma unroll
;                     for (int e = 3; e < 15; e += 2) mx = fmaxf(fmaxf(mx, s[e]), s[e + 1]);
;                     mx = fmaxf(mx, s[15]);
;                     mx = fmaxf(mx, __shfl_xor(mx, 32));
;                     if (__any(mx > m + 8.0f)) { const float mn = fmaxf(m, mx), alpha = __builtin_amdgcn_exp2f(m - mn); l *= alpha; m = mn;
; #pragma unroll
;                         for (int db = 0; db < 4; ++db)
; #pragma unroll
;                             for (int e = 0; e < 16; ++e) o[db][e] *= alpha; }
.LBB0_605:
	s_nop 1
	v_max_f32_e32 v178, v67, v67
	v_max_f32_e32 v187, v66, v66
	v_max_f32_e32 v178, v187, v178
	v_max3_f32 v178, v178, v68, v69
	v_max3_f32 v178, v178, v70, v71
	v_max3_f32 v178, v178, v72, v73
	v_max3_f32 v178, v178, v74, v75
	v_max3_f32 v178, v178, v76, v77
	v_max3_f32 v178, v178, v78, v79
	v_and_b32_e32 v233, 64, v231
	v_max3_f32 v187, v178, v80, v81
	v_xor_b32_e32 v178, 32, v231
	v_add_u32_e32 v233, 64, v233
	v_cmp_lt_i32_e32 vcc, v178, v233
	s_nop 1
	v_cndmask_b32_e32 v178, v231, v178, vcc
	v_lshlrev_b32_e32 v178, 2, v178
	v_mov_b32_e32 v233, v187
	s_nop 1
	v_permlane32_swap_b32_e32 v233, v187
	s_waitcnt lgkmcnt(0)
	v_max_f32_e32 v233, v233, v233
	v_max_f32_e32 v187, v187, v233
	v_add_f32_e32 v233, 0x41000000, v194
	v_cmp_gt_f32_e32 vcc, v187, v233
	s_cbranch_vccz .LBB0_607
	v_max_f32_e32 v187, v187, v187
	v_max_f32_e32 v233, v194, v194
	v_max_f32_e32 v187, v233, v187
	v_sub_f32_e32 v194, v194, v187
	v_exp_f32_e32 v194, v194
	s_nop 0
	v_pk_mul_f32 v[16:17], v[16:17], v[194:195] op_sel_hi:[1,0]
	v_pk_mul_f32 v[14:15], v[14:15], v[194:195] op_sel_hi:[1,0]
	v_pk_mul_f32 v[12:13], v[12:13], v[194:195] op_sel_hi:[1,0]
	v_pk_mul_f32 v[10:11], v[10:11], v[194:195] op_sel_hi:[1,0]
	v_pk_mul_f32 v[8:9], v[8:9], v[194:195] op_sel_hi:[1,0]
	v_pk_mul_f32 v[6:7], v[6:7], v[194:195] op_sel_hi:[1,0]
	v_pk_mul_f32 v[4:5], v[4:5], v[194:195] op_sel_hi:[1,0]
	v_pk_mul_f32 v[2:3], v[2:3], v[194:195] op_sel_hi:[1,0]
	v_pk_mul_f32 v[32:33], v[32:33], v[194:195] op_sel_hi:[1,0]
	v_pk_mul_f32 v[30:31], v[30:31], v[194:195] op_sel_hi:[1,0]
	v_pk_mul_f32 v[28:29], v[28:29], v[194:195] op_sel_hi:[1,0]
	v_pk_mul_f32 v[26:27], v[26:27], v[194:195] op_sel_hi:[1,0]
	v_pk_mul_f32 v[24:25], v[24:25], v[194:195] op_sel_hi:[1,0]
	v_pk_mul_f32 v[22:23], v[22:23], v[194:195] op_sel_hi:[1,0]
	v_pk_mul_f32 v[20:21], v[20:21], v[194:195] op_sel_hi:[1,0]
	v_pk_mul_f32 v[18:19], v[18:19], v[194:195] op_sel_hi:[1,0]
	v_pk_mul_f32 v[48:49], v[48:49], v[194:195] op_sel_hi:[1,0]
	v_pk_mul_f32 v[46:47], v[46:47], v[194:195] op_sel_hi:[1,0]
	v_pk_mul_f32 v[44:45], v[44:45], v[194:195] op_sel_hi:[1,0]
	v_pk_mul_f32 v[42:43], v[42:43], v[194:195] op_sel_hi:[1,0]
	v_pk_mul_f32 v[40:41], v[40:41], v[194:195] op_sel_hi:[1,0]
	v_pk_mul_f32 v[38:39], v[38:39], v[194:195] op_sel_hi:[1,0]
	v_pk_mul_f32 v[36:37], v[36:37], v[194:195] op_sel_hi:[1,0]
	v_pk_mul_f32 v[34:35], v[34:35], v[194:195] op_sel_hi:[1,0]
	v_pk_mul_f32 v[64:65], v[64:65], v[194:195] op_sel_hi:[1,0]
	v_pk_mul_f32 v[62:63], v[62:63], v[194:195] op_sel_hi:[1,0]
	v_pk_mul_f32 v[60:61], v[60:61], v[194:195] op_sel_hi:[1,0]
	v_pk_mul_f32 v[58:59], v[58:59], v[194:195] op_sel_hi:[1,0]
	v_pk_mul_f32 v[56:57], v[56:57], v[194:195] op_sel_hi:[1,0]
	v_pk_mul_f32 v[54:55], v[54:55], v[194:195] op_sel_hi:[1,0]
	v_pk_mul_f32 v[52:53], v[52:53], v[194:195] op_sel_hi:[1,0]
	v_pk_mul_f32 v[50:51], v[50:51], v[194:195] op_sel_hi:[1,0]
	v_mul_f32_e32 v195, v195, v194
	v_mov_b32_e32 v194, v187
; DI unsigned cvtpk(float lo, float hi) { f32x2 v = {lo, hi}; bf16x2_t b = __builtin_convertvector(v, bf16x2_t); return __builtin_bit_cast(unsigned, b); }
; DI f32x16 mfma32(bf16x8 a, bf16x8 b, f32x16 c) { return __builtin_amdgcn_mfma_f32_32x32x16_bf16(a, b, c, 0, 0, 0); }
; template <int DIL, bool FIRST, bool LAST>
; DI void attn_phase(Frame& F) {
;     ...
;                     float rs = 0.f;
; #pragma unroll
;                     for (int e = 0; e < 16; ++e) { s[e] = __builtin_amdgcn_exp2f(s[e] - m); rs += s[e]; }
;                     rs += __shfl_xor(rs, 32); l += rs;
;                     bf16x8 pb[2];
; #pragma unroll
;                     for (int s2 = 0; s2 < 2; ++s2) { u32x4 w; w.x = cvtpk(s[8 * s2], s[8 * s2 + 1]); w.y = cvtpk(s[8 * s2 + 2], s[8 * s2 + 3]); w.z = cvtpk(s[8 * s2 + 4], s[8 * s2 + 5]); w.w = cvtpk(s[8 * s2 + 6], s[8 * s2 + 7]);
;                         pb[s2] = __builtin_bit_cast(bf16x8, w); }
; #pragma unroll
;                     for (int s2 = 0; s2 < 2; ++s2) {
; #pragma unroll
;                         for (int db = 0; db < 4; ++db) o[db] = mfma32(va[s2][db], pb[s2], o[db]);
;                     }
;     ...
;                         } else {
;                             bf16* ostp = OST + hrow * 128 + 8 * h; float* mlp = ML + hrow * 2;
; #pragma unroll
;                             for (int db = 0; db < 4; ++db)
; #pragma unroll
;                                 for (int j2 = 0; j2 < 2; ++j2) { u32x2 w2[2];
; #pragma unroll
;                                     for (int q2 = 0; q2 < 2; ++q2) { const int g4 = 2 * j2 + q2; w2[q2].x = cvtpk(o[db][4 * g4], o[db][4 * g4 + 1]); w2[q2].y = cvtpk(o[db][4 * g4 + 2], o[db][4 * g4 + 3]); }
;                                     swap32(w2[0], w2[1]); u32x4 w; w.x = w2[0].x; w.y = w2[0].y; w.z = w2[1].x; w.w = w2[1].y;
;                                     *(u32x4*)(ostp + 32 * db + 16 * j2) = w; }
;                             if (h == 0) { f32x2 mlv; mlv[0] = m; mlv[1] = l; *(f32x2*)mlp = mlv; }
.LBB0_607:
	v_sub_f32_e32 v66, v66, v194
	v_exp_f32_e32 v66, v66
	v_sub_f32_e32 v67, v67, v194
	v_exp_f32_e32 v67, v67
	v_sub_f32_e32 v68, v68, v194
	v_exp_f32_e32 v68, v68
	v_sub_f32_e32 v69, v69, v194
	v_exp_f32_e32 v69, v69
	v_sub_f32_e32 v70, v70, v194
	v_add_f32_e32 v187, 0, v66
	v_exp_f32_e32 v70, v70
	v_sub_f32_e32 v71, v71, v194
	v_add_f32_e32 v187, v67, v187
	v_exp_f32_e32 v71, v71
	v_sub_f32_e32 v72, v72, v194
	v_sub_f32_e32 v73, v73, v194
	v_add_f32_e32 v187, v68, v187
	v_exp_f32_e32 v72, v72
	v_exp_f32_e32 v73, v73
	v_add_f32_e32 v187, v69, v187
	v_sub_f32_e32 v74, v74, v194
	v_add_f32_e32 v187, v70, v187
	v_exp_f32_e32 v74, v74
	v_sub_f32_e32 v75, v75, v194
	v_add_f32_e32 v187, v71, v187
	v_exp_f32_e32 v75, v75
	v_sub_f32_e32 v76, v76, v194
	v_add_f32_e32 v187, v72, v187
	v_exp_f32_e32 v76, v76
	v_sub_f32_e32 v77, v77, v194
	v_cvt_pk_bf16_f32 v66, v66, v67
	v_cvt_pk_bf16_f32 v67, v68, v69
	v_cvt_pk_bf16_f32 v68, v70, v71
	v_cvt_pk_bf16_f32 v69, v72, v73
	v_add_f32_e32 v187, v73, v187
	v_exp_f32_e32 v77, v77
	v_sub_f32_e32 v78, v78, v194
	v_mfma_f32_32x32x16_bf16 v[2:17], v[170:173], v[66:69], v[2:17]
	v_add_f32_e32 v187, v74, v187
	v_exp_f32_e32 v78, v78
	v_sub_f32_e32 v79, v79, v194
	v_add_f32_e32 v187, v75, v187
	v_exp_f32_e32 v79, v79
	v_sub_f32_e32 v80, v80, v194
	v_sub_f32_e32 v81, v81, v194
	v_mfma_f32_32x32x16_bf16 v[18:33], v[174:177], v[66:69], v[18:33]
	v_add_f32_e32 v187, v76, v187
	v_exp_f32_e32 v80, v80
	v_exp_f32_e32 v81, v81
	v_add_f32_e32 v187, v77, v187
	v_add_f32_e32 v187, v78, v187
	v_add_f32_e32 v187, v79, v187
	v_add_f32_e32 v187, v80, v187
	v_mfma_f32_32x32x16_bf16 v[34:49], v[166:169], v[66:69], v[34:49]
	v_cvt_pk_bf16_f32 v70, v74, v75
	v_cvt_pk_bf16_f32 v71, v76, v77
	v_cvt_pk_bf16_f32 v72, v78, v79
	v_cvt_pk_bf16_f32 v73, v80, v81
	v_add_f32_e32 v187, v81, v187
	v_mov_b32_e32 v178, v187
	s_nop 1
	v_permlane32_swap_b32_e32 v178, v187
	s_andn2_b64 vcc, exec, s[86:87]
	v_mfma_f32_32x32x16_bf16 v[50:65], v[162:165], v[66:69], v[50:65]
	s_waitcnt lgkmcnt(0)
	v_add_f32_e32 v178, v187, v178
	v_add_f32_e32 v195, v195, v178
	v_mfma_f32_32x32x16_bf16 v[2:17], v[158:161], v[70:73], v[2:17]
	v_mfma_f32_32x32x16_bf16 v[18:33], v[154:157], v[70:73], v[18:33]
	v_mfma_f32_32x32x16_bf16 v[34:49], v[150:153], v[70:73], v[34:49]
	v_mfma_f32_32x32x16_bf16 v[50:65], v[146:149], v[70:73], v[50:65]
	s_cbranch_vccnz .LBB0_589
	v_or_b32_e32 v66, s5, v1
	v_ashrrev_i32_e32 v67, 31, v66
	v_lshl_add_u64 v[66:67], v[66:67], 2, s[82:83]
	v_lshlrev_b64 v[68:69], 8, v[66:67]
	v_lshl_add_u64 v[72:73], v[182:183], 0, v[68:69]
	s_nop 2
	v_cvt_pk_bf16_f32 v68, v2, v3
	v_cvt_pk_bf16_f32 v69, v4, v5
	v_cvt_pk_bf16_f32 v70, v6, v7
	v_cvt_pk_bf16_f32 v71, v8, v9
	s_nop 0
	v_permlane32_swap_b32_e32 v68, v70
	v_permlane32_swap_b32_e32 v69, v71
	global_store_dwordx4 v[72:73], v[68:71], off
	s_nop 1
	v_cvt_pk_bf16_f32 v68, v10, v11
	v_cvt_pk_bf16_f32 v69, v12, v13
	v_cvt_pk_bf16_f32 v70, v14, v15
	v_cvt_pk_bf16_f32 v71, v16, v17
	s_nop 0
	v_permlane32_swap_b32_e32 v68, v70
	v_permlane32_swap_b32_e32 v69, v71
	global_store_dwordx4 v[72:73], v[68:71], off offset:32
	s_nop 1
	v_cvt_pk_bf16_f32 v68, v18, v19
	v_cvt_pk_bf16_f32 v69, v20, v21
	v_cvt_pk_bf16_f32 v70, v22, v23
	v_cvt_pk_bf16_f32 v71, v24, v25
	s_nop 0
	v_permlane32_swap_b32_e32 v68, v70
	v_permlane32_swap_b32_e32 v69, v71
	global_store_dwordx4 v[72:73], v[68:71], off offset:64
	s_nop 1
	v_cvt_pk_bf16_f32 v68, v26, v27
	v_cvt_pk_bf16_f32 v69, v28, v29
	v_cvt_pk_bf16_f32 v70, v30, v31
	v_cvt_pk_bf16_f32 v71, v32, v33
	s_nop 0
	v_permlane32_swap_b32_e32 v68, v70
	v_permlane32_swap_b32_e32 v69, v71
	global_store_dwordx4 v[72:73], v[68:71], off offset:96
	s_nop 1
	v_cvt_pk_bf16_f32 v68, v34, v35
	v_cvt_pk_bf16_f32 v69, v36, v37
	v_cvt_pk_bf16_f32 v70, v38, v39
	v_cvt_pk_bf16_f32 v71, v40, v41
	s_nop 0
	v_permlane32_swap_b32_e32 v68, v70
	v_permlane32_swap_b32_e32 v69, v71
	global_store_dwordx4 v[72:73], v[68:71], off offset:128
	s_nop 1
	v_cvt_pk_bf16_f32 v68, v42, v43
	v_cvt_pk_bf16_f32 v69, v44, v45
	v_cvt_pk_bf16_f32 v70, v46, v47
	v_cvt_pk_bf16_f32 v71, v48, v49
	s_nop 0
	v_permlane32_swap_b32_e32 v68, v70
	v_permlane32_swap_b32_e32 v69, v71
	global_store_dwordx4 v[72:73], v[68:71], off offset:160
	s_nop 1
	v_cvt_pk_bf16_f32 v68, v50, v51
	v_cvt_pk_bf16_f32 v69, v52, v53
	v_cvt_pk_bf16_f32 v70, v54, v55
	v_cvt_pk_bf16_f32 v71, v56, v57
	s_nop 0
	v_permlane32_swap_b32_e32 v68, v70
	v_permlane32_swap_b32_e32 v69, v71
	global_store_dwordx4 v[72:73], v[68:71], off offset:192
	s_nop 1
	v_cvt_pk_bf16_f32 v68, v58, v59
	v_cvt_pk_bf16_f32 v69, v60, v61
	v_cvt_pk_bf16_f32 v70, v62, v63
	v_cvt_pk_bf16_f32 v71, v64, v65
	s_nop 0
	v_permlane32_swap_b32_e32 v68, v70
	v_permlane32_swap_b32_e32 v69, v71
	global_store_dwordx4 v[72:73], v[68:71], off offset:224
	s_mov_b64 s[0:1], exec
	v_readlane_b32 s6, v254, 54
	v_readlane_b32 s7, v254, 55
	s_and_b64 s[6:7], s[0:1], s[6:7]
	s_mov_b64 exec, s[6:7]
	s_cbranch_execnz .LBB0_611
	s_or_b64 exec, exec, s[0:1]
	s_cmp_gt_i32 s3, 2
	s_mov_b64 s[0:1], -1
	s_cbranch_scc1 .LBB0_612

; DI unsigned cvtpk(float lo, float hi) { f32x2 v = {lo, hi}; bf16x2_t b = __builtin_convertvector(v, bf16x2_t); return __builtin_bit_cast(unsigned, b); }
; DI f32x16 mfma32(bf16x8 a, bf16x8 b, f32x16 c) { return __builtin_amdgcn_mfma_f32_32x32x16_bf16(a, b, c, 0, 0, 0); }
; template <int DIL, bool FIRST, bool LAST>
; DI void attn_phase(Frame& F) {
;     ...
;                     float mx = fmaxf(fmaxf(s[0], s[1]), s[2]);
; #pragma unroll
;                     for (int e = 3; e < 15; e += 2) mx = fmaxf(fmaxf(mx, s[e]), s[e + 1]);
;                     mx = fmaxf(mx, s[15]);
;                     mx = fmaxf(mx, __shfl_xor(mx, 32));
;                     if (__any(mx > m + 8.0f)) { const float mn = fmaxf(m, mx), alpha = __builtin_amdgcn_exp2f(m - mn); l *= alpha; m = mn;
; #pragma unroll
;                         for (int db = 0; db < 4; ++db)
; #pragma unroll
;                             for (int e = 0; e < 16; ++e) o[db][e] *= alpha; }
;                     float rs = 0.f;
; #pragma unroll
;                     for (int e = 0; e < 16; ++e) { s[e] = __builtin_amdgcn_exp2f(s[e] - m); rs += s[e]; }
;                     rs += __shfl_xor(rs, 32); l += rs;
;                     bf16x8 pb[2];
; #pragma unroll
;                     for (int s2 = 0; s2 < 2; ++s2) { u32x4 w; w.x = cvtpk(s[8 * s2], s[8 * s2 + 1]); w.y = cvtpk(s[8 * s2 + 2], s[8 * s2 + 3]); w.z = cvtpk(s[8 * s2 + 4], s[8 * s2 + 5]); w.w = cvtpk(s[8 * s2 + 6], s[8 * s2 + 7]);
;                         pb[s2] = __builtin_bit_cast(bf16x8, w); }
; #pragma unroll
;                     for (int s2 = 0; s2 < 2; ++s2) {
; #pragma unroll
;                         for (int db = 0; db < 4; ++db) o[db] = mfma32(va[s2][db], pb[s2], o[db]);
;                     }
.LBB0_710:
	s_nop 1
	v_max_f32_e32 v178, v67, v67
	v_max_f32_e32 v191, v66, v66
	v_max_f32_e32 v178, v191, v178
	v_max3_f32 v178, v178, v68, v69
	v_max3_f32 v178, v178, v70, v71
	v_max3_f32 v178, v178, v72, v73
	v_max3_f32 v178, v178, v74, v75
	v_max3_f32 v178, v178, v76, v77
	v_max3_f32 v178, v178, v78, v79
	v_and_b32_e32 v237, 64, v234
	v_max3_f32 v191, v178, v80, v81
	v_xor_b32_e32 v178, 32, v234
	v_add_u32_e32 v237, 64, v237
	v_cmp_lt_i32_e32 vcc, v178, v237
	s_nop 1
	v_cndmask_b32_e32 v178, v234, v178, vcc
	v_lshlrev_b32_e32 v178, 2, v178
	v_mov_b32_e32 v237, v191
	s_nop 1
	v_permlane32_swap_b32_e32 v237, v191
	s_waitcnt lgkmcnt(0)
	v_max_f32_e32 v237, v237, v237
	v_max_f32_e32 v191, v191, v237
	v_add_f32_e32 v237, 0x41000000, v236
	v_cmp_gt_f32_e32 vcc, v191, v237
	s_cbranch_vccz .LBB0_712
	v_max_f32_e32 v191, v191, v191
	v_max_f32_e32 v237, v236, v236
	v_max_f32_e32 v191, v237, v191
	v_sub_f32_e32 v236, v236, v191
	v_exp_f32_e32 v236, v236
	s_nop 0
	v_pk_mul_f32 v[16:17], v[16:17], v[236:237] op_sel_hi:[1,0]
	v_pk_mul_f32 v[14:15], v[14:15], v[236:237] op_sel_hi:[1,0]
	v_pk_mul_f32 v[12:13], v[12:13], v[236:237] op_sel_hi:[1,0]
	v_pk_mul_f32 v[10:11], v[10:11], v[236:237] op_sel_hi:[1,0]
	v_pk_mul_f32 v[8:9], v[8:9], v[236:237] op_sel_hi:[1,0]
	v_pk_mul_f32 v[6:7], v[6:7], v[236:237] op_sel_hi:[1,0]
	v_pk_mul_f32 v[4:5], v[4:5], v[236:237] op_sel_hi:[1,0]
	v_pk_mul_f32 v[2:3], v[2:3], v[236:237] op_sel_hi:[1,0]
	v_pk_mul_f32 v[32:33], v[32:33], v[236:237] op_sel_hi:[1,0]
	v_pk_mul_f32 v[30:31], v[30:31], v[236:237] op_sel_hi:[1,0]
	v_pk_mul_f32 v[28:29], v[28:29], v[236:237] op_sel_hi:[1,0]
	v_pk_mul_f32 v[26:27], v[26:27], v[236:237] op_sel_hi:[1,0]
	v_pk_mul_f32 v[24:25], v[24:25], v[236:237] op_sel_hi:[1,0]
	v_pk_mul_f32 v[22:23], v[22:23], v[236:237] op_sel_hi:[1,0]
	v_pk_mul_f32 v[20:21], v[20:21], v[236:237] op_sel_hi:[1,0]
	v_pk_mul_f32 v[18:19], v[18:19], v[236:237] op_sel_hi:[1,0]
	v_pk_mul_f32 v[48:49], v[48:49], v[236:237] op_sel_hi:[1,0]
	v_pk_mul_f32 v[46:47], v[46:47], v[236:237] op_sel_hi:[1,0]
	v_pk_mul_f32 v[44:45], v[44:45], v[236:237] op_sel_hi:[1,0]
	v_pk_mul_f32 v[42:43], v[42:43], v[236:237] op_sel_hi:[1,0]
	v_pk_mul_f32 v[40:41], v[40:41], v[236:237] op_sel_hi:[1,0]
	v_pk_mul_f32 v[38:39], v[38:39], v[236:237] op_sel_hi:[1,0]
	v_pk_mul_f32 v[36:37], v[36:37], v[236:237] op_sel_hi:[1,0]
	v_pk_mul_f32 v[34:35], v[34:35], v[236:237] op_sel_hi:[1,0]
	v_pk_mul_f32 v[64:65], v[64:65], v[236:237] op_sel_hi:[1,0]
	v_pk_mul_f32 v[62:63], v[62:63], v[236:237] op_sel_hi:[1,0]
	v_pk_mul_f32 v[60:61], v[60:61], v[236:237] op_sel_hi:[1,0]
	v_pk_mul_f32 v[58:59], v[58:59], v[236:237] op_sel_hi:[1,0]
	v_pk_mul_f32 v[56:57], v[56:57], v[236:237] op_sel_hi:[1,0]
	v_pk_mul_f32 v[54:55], v[54:55], v[236:237] op_sel_hi:[1,0]
	v_pk_mul_f32 v[52:53], v[52:53], v[236:237] op_sel_hi:[1,0]
	v_pk_mul_f32 v[50:51], v[50:51], v[236:237] op_sel_hi:[1,0]
	v_mul_f32_e32 v235, v235, v236
	v_mov_b32_e32 v236, v191
.LBB0_712:
	v_sub_f32_e32 v66, v66, v236
	v_exp_f32_e32 v66, v66
	v_sub_f32_e32 v67, v67, v236
	v_exp_f32_e32 v67, v67
	v_sub_f32_e32 v68, v68, v236
	v_exp_f32_e32 v68, v68
	v_sub_f32_e32 v69, v69, v236
	v_exp_f32_e32 v69, v69
	v_sub_f32_e32 v70, v70, v236
	v_add_f32_e32 v191, 0, v66
	v_exp_f32_e32 v70, v70
	v_sub_f32_e32 v71, v71, v236
	v_add_f32_e32 v191, v67, v191
	v_exp_f32_e32 v71, v71
	v_sub_f32_e32 v72, v72, v236
	v_sub_f32_e32 v73, v73, v236
	v_add_f32_e32 v191, v68, v191
	v_exp_f32_e32 v72, v72
	v_exp_f32_e32 v73, v73
	v_add_f32_e32 v191, v69, v191
	v_sub_f32_e32 v74, v74, v236
	v_add_f32_e32 v191, v70, v191
	v_exp_f32_e32 v74, v74
	v_sub_f32_e32 v75, v75, v236
	v_add_f32_e32 v191, v71, v191
	v_exp_f32_e32 v75, v75
	v_sub_f32_e32 v76, v76, v236
	v_add_f32_e32 v191, v72, v191
	v_exp_f32_e32 v76, v76
	v_sub_f32_e32 v77, v77, v236
	v_cvt_pk_bf16_f32 v66, v66, v67
	v_cvt_pk_bf16_f32 v67, v68, v69
	v_cvt_pk_bf16_f32 v68, v70, v71
	v_cvt_pk_bf16_f32 v69, v72, v73
	v_add_f32_e32 v191, v73, v191
	v_exp_f32_e32 v77, v77
	v_sub_f32_e32 v78, v78, v236
	v_mfma_f32_32x32x16_bf16 v[2:17], v[170:173], v[66:69], v[2:17]
	v_add_f32_e32 v191, v74, v191
	v_exp_f32_e32 v78, v78
	v_sub_f32_e32 v79, v79, v236
	v_add_f32_e32 v191, v75, v191
	v_exp_f32_e32 v79, v79
	v_sub_f32_e32 v80, v80, v236
	v_sub_f32_e32 v81, v81, v236
	v_mfma_f32_32x32x16_bf16 v[18:33], v[174:177], v[66:69], v[18:33]
	v_add_f32_e32 v191, v76, v191
	v_exp_f32_e32 v80, v80
	v_exp_f32_e32 v81, v81
	v_add_f32_e32 v191, v77, v191
	v_add_f32_e32 v191, v78, v191
	v_add_f32_e32 v191, v79, v191
	v_add_f32_e32 v191, v80, v191
	v_mfma_f32_32x32x16_bf16 v[34:49], v[166:169], v[66:69], v[34:49]
	v_cvt_pk_bf16_f32 v70, v74, v75
	v_cvt_pk_bf16_f32 v71, v76, v77
	v_cvt_pk_bf16_f32 v72, v78, v79
	v_cvt_pk_bf16_f32 v73, v80, v81
	v_add_f32_e32 v191, v81, v191
	v_mov_b32_e32 v178, v191
	s_nop 1
	v_permlane32_swap_b32_e32 v178, v191
	s_andn2_b64 vcc, exec, s[86:87]
	v_mfma_f32_32x32x16_bf16 v[50:65], v[162:165], v[66:69], v[50:65]
	s_waitcnt lgkmcnt(0)
	v_add_f32_e32 v178, v191, v178
	v_add_f32_e32 v235, v235, v178
	v_mfma_f32_32x32x16_bf16 v[2:17], v[158:161], v[70:73], v[2:17]
	v_mfma_f32_32x32x16_bf16 v[18:33], v[154:157], v[70:73], v[18:33]
	v_mfma_f32_32x32x16_bf16 v[34:49], v[150:153], v[70:73], v[34:49]
	v_mfma_f32_32x32x16_bf16 v[50:65], v[146:149], v[70:73], v[50:65]
	s_cbranch_vccnz .LBB0_694
; DI unsigned cvtpk(float lo, float hi) { f32x2 v = {lo, hi}; bf16x2_t b = __builtin_convertvector(v, bf16x2_t); return __builtin_bit_cast(unsigned, b); }
; template <int DIL, bool FIRST, bool LAST>
; DI void attn_phase(Frame& F) {
;     ...
;                             const float il = 1.0f / l;
;                             bf16* mp = MIX + rowq * DM + hd * 128 + 8 * h;
; #pragma unroll
;                             for (int db = 0; db < 4; ++db)
; #pragma unroll
;                                 for (int j2 = 0; j2 < 2; ++j2) { u32x2 w2[2];
; #pragma unroll
;                                     for (int q2 = 0; q2 < 2; ++q2) { const int g4 = 2 * j2 + q2; w2[q2].x = cvtpk(o[db][4 * g4] * il, o[db][4 * g4 + 1] * il); w2[q2].y = cvtpk(o[db][4 * g4 + 2] * il, o[db][4 * g4 + 3] * il); }
;                                     swap32(w2[0], w2[1]); u32x4 w; w.x = w2[0].x; w.y = w2[0].y; w.z = w2[1].x; w.w = w2[1].y;
;                                     *(u32x4*)(mp + 32 * db + 16 * j2) = w; }
;                         } else {
;                             bf16* ostp = OST + hrow * 128 + 8 * h; float* mlp = ML + hrow * 2;
; #pragma unroll
;                             for (int db = 0; db < 4; ++db)
; #pragma unroll
;                                 for (int j2 = 0; j2 < 2; ++j2) { u32x2 w2[2];
; #pragma unroll
;                                     for (int q2 = 0; q2 < 2; ++q2) { const int g4 = 2 * j2 + q2; w2[q2].x = cvtpk(o[db][4 * g4], o[db][4 * g4 + 1]); w2[q2].y = cvtpk(o[db][4 * g4 + 2], o[db][4 * g4 + 3]); }
;                                     swap32(w2[0], w2[1]); u32x4 w; w.x = w2[0].x; w.y = w2[0].y; w.z = w2[1].x; w.w = w2[1].y;
;                                     *(u32x4*)(ostp + 32 * db + 16 * j2) = w; }
;                             if (h == 0) { f32x2 mlv; mlv[0] = m; mlv[1] = l; *(f32x2*)mlp = mlv; }
;                         }
;                         if (mq < 3) ATT_PREFETCH(k, qt + 8); else if (k + 1 < nun) ATT_PREFETCH(k + 1, F.wave);
	v_div_scale_f32 v68, s[0:1], v235, v235, 1.0
	v_rcp_f32_e32 v69, v68
	v_or_b32_e32 v66, s97, v207
	v_ashrrev_i32_e32 v67, 31, v66
	v_lshlrev_b64 v[66:67], 16, v[66:67]
	v_fma_f32 v70, -v68, v69, 1.0
	v_fmac_f32_e32 v69, v70, v69
	v_div_scale_f32 v70, vcc, 1.0, v235, 1.0
	v_mul_f32_e32 v71, v70, v69
	v_fma_f32 v72, -v68, v71, v70
	v_fmac_f32_e32 v71, v72, v69
	v_fma_f32 v68, -v68, v71, v70
	v_div_fmas_f32 v68, v68, v69, v71
	v_div_fixup_f32 v70, v68, v235, 1.0
	v_lshl_add_u64 v[72:73], v[192:193], 0, v[66:67]
	v_pk_mul_f32 v[66:67], v[2:3], v[70:71] op_sel_hi:[1,0]
	v_pk_mul_f32 v[68:69], v[4:5], v[70:71] op_sel_hi:[1,0]
	v_cvt_pk_bf16_f32 v66, v66, v67
	v_cvt_pk_bf16_f32 v67, v68, v69
	v_pk_mul_f32 v[68:69], v[6:7], v[70:71] op_sel_hi:[1,0]
	v_pk_mul_f32 v[74:75], v[8:9], v[70:71] op_sel_hi:[1,0]
	v_cvt_pk_bf16_f32 v68, v68, v69
	v_cvt_pk_bf16_f32 v69, v74, v75
	s_nop 0
	v_permlane32_swap_b32_e32 v66, v68
	v_permlane32_swap_b32_e32 v67, v69
	global_store_dwordx4 v[72:73], v[66:69], off
	v_pk_mul_f32 v[74:75], v[16:17], v[70:71] op_sel_hi:[1,0]
	s_cmp_gt_i32 s77, 2
	v_pk_mul_f32 v[66:67], v[10:11], v[70:71] op_sel_hi:[1,0]
	v_pk_mul_f32 v[68:69], v[12:13], v[70:71] op_sel_hi:[1,0]
	v_cvt_pk_bf16_f32 v66, v66, v67
	v_cvt_pk_bf16_f32 v67, v68, v69
	v_pk_mul_f32 v[68:69], v[14:15], v[70:71] op_sel_hi:[1,0]
	s_mov_b64 s[0:1], -1
	v_cvt_pk_bf16_f32 v68, v68, v69
	v_cvt_pk_bf16_f32 v69, v74, v75
	s_nop 0
	v_permlane32_swap_b32_e32 v66, v68
	v_permlane32_swap_b32_e32 v67, v69
	global_store_dwordx4 v[72:73], v[66:69], off offset:32
	v_pk_mul_f32 v[74:75], v[24:25], v[70:71] op_sel_hi:[1,0]
	s_nop 0
	v_pk_mul_f32 v[66:67], v[18:19], v[70:71] op_sel_hi:[1,0]
	v_pk_mul_f32 v[68:69], v[20:21], v[70:71] op_sel_hi:[1,0]
	v_cvt_pk_bf16_f32 v66, v66, v67
	v_cvt_pk_bf16_f32 v67, v68, v69
	v_pk_mul_f32 v[68:69], v[22:23], v[70:71] op_sel_hi:[1,0]
	s_nop 0
	v_cvt_pk_bf16_f32 v68, v68, v69
	v_cvt_pk_bf16_f32 v69, v74, v75
	s_nop 0
	v_permlane32_swap_b32_e32 v66, v68
	v_permlane32_swap_b32_e32 v67, v69
	global_store_dwordx4 v[72:73], v[66:69], off offset:64
	v_pk_mul_f32 v[74:75], v[32:33], v[70:71] op_sel_hi:[1,0]
	s_nop 0
	v_pk_mul_f32 v[66:67], v[26:27], v[70:71] op_sel_hi:[1,0]
	v_pk_mul_f32 v[68:69], v[28:29], v[70:71] op_sel_hi:[1,0]
	v_cvt_pk_bf16_f32 v66, v66, v67
	v_cvt_pk_bf16_f32 v67, v68, v69
	v_pk_mul_f32 v[68:69], v[30:31], v[70:71] op_sel_hi:[1,0]
	s_nop 0
	v_cvt_pk_bf16_f32 v68, v68, v69
	v_cvt_pk_bf16_f32 v69, v74, v75
	s_nop 0
	v_permlane32_swap_b32_e32 v66, v68
	v_permlane32_swap_b32_e32 v67, v69
	global_store_dwordx4 v[72:73], v[66:69], off offset:96
	v_pk_mul_f32 v[74:75], v[40:41], v[70:71] op_sel_hi:[1,0]
	s_nop 0
	v_pk_mul_f32 v[66:67], v[34:35], v[70:71] op_sel_hi:[1,0]
	v_pk_mul_f32 v[68:69], v[36:37], v[70:71] op_sel_hi:[1,0]
	v_cvt_pk_bf16_f32 v66, v66, v67
	v_cvt_pk_bf16_f32 v67, v68, v69
	v_pk_mul_f32 v[68:69], v[38:39], v[70:71] op_sel_hi:[1,0]
	s_nop 0
	v_cvt_pk_bf16_f32 v68, v68, v69
	v_cvt_pk_bf16_f32 v69, v74, v75
	s_nop 0
	v_permlane32_swap_b32_e32 v66, v68
	v_permlane32_swap_b32_e32 v67, v69
	global_store_dwordx4 v[72:73], v[66:69], off offset:128
	v_pk_mul_f32 v[74:75], v[48:49], v[70:71] op_sel_hi:[1,0]
	s_nop 0
	v_pk_mul_f32 v[66:67], v[42:43], v[70:71] op_sel_hi:[1,0]
	v_pk_mul_f32 v[68:69], v[44:45], v[70:71] op_sel_hi:[1,0]
	v_cvt_pk_bf16_f32 v66, v66, v67
	v_cvt_pk_bf16_f32 v67, v68, v69
	v_pk_mul_f32 v[68:69], v[46:47], v[70:71] op_sel_hi:[1,0]
	s_nop 0
	v_cvt_pk_bf16_f32 v68, v68, v69
	v_cvt_pk_bf16_f32 v69, v74, v75
	s_nop 0
	v_permlane32_swap_b32_e32 v66, v68
	v_permlane32_swap_b32_e32 v67, v69
	global_store_dwordx4 v[72:73], v[66:69], off offset:160
	v_pk_mul_f32 v[74:75], v[56:57], v[70:71] op_sel_hi:[1,0]
	s_nop 0
	v_pk_mul_f32 v[66:67], v[50:51], v[70:71] op_sel_hi:[1,0]
	v_pk_mul_f32 v[68:69], v[52:53], v[70:71] op_sel_hi:[1,0]
	v_cvt_pk_bf16_f32 v66, v66, v67
	v_cvt_pk_bf16_f32 v67, v68, v69
	v_pk_mul_f32 v[68:69], v[54:55], v[70:71] op_sel_hi:[1,0]
	s_nop 0
	v_cvt_pk_bf16_f32 v68, v68, v69
	v_cvt_pk_bf16_f32 v69, v74, v75
	s_nop 0
	v_permlane32_swap_b32_e32 v66, v68
	v_permlane32_swap_b32_e32 v67, v69
	global_store_dwordx4 v[72:73], v[66:69], off offset:192
	s_nop 1
	v_pk_mul_f32 v[66:67], v[58:59], v[70:71] op_sel_hi:[1,0]
	v_pk_mul_f32 v[68:69], v[60:61], v[70:71] op_sel_hi:[1,0]
	v_cvt_pk_bf16_f32 v66, v66, v67
	v_cvt_pk_bf16_f32 v67, v68, v69
	v_pk_mul_f32 v[68:69], v[62:63], v[70:71] op_sel_hi:[1,0]
	v_pk_mul_f32 v[70:71], v[64:65], v[70:71] op_sel_hi:[1,0]
	v_cvt_pk_bf16_f32 v68, v68, v69
	v_cvt_pk_bf16_f32 v69, v70, v71
	s_nop 0
	v_permlane32_swap_b32_e32 v66, v68
	v_permlane32_swap_b32_e32 v67, v69
	global_store_dwordx4 v[72:73], v[66:69], off offset:224
	s_cbranch_scc0 .LBB0_717
	v_readlane_b32 s0, v254, 54
	v_readlane_b32 s1, v254, 55
	s_andn2_b64 vcc, exec, s[0:1]
	s_cbranch_vccnz .LBB0_716
	global_load_dwordx4 v[82:85], v[194:195], off offset:0 nt
	global_load_dwordx4 v[86:89], v[194:195], off offset:32 nt
	global_load_dwordx4 v[90:93], v[194:195], off offset:64 nt
	global_load_dwordx4 v[94:97], v[194:195], off offset:0x60 nt
	global_load_dwordx4 v[98:101], v[194:195], off offset:0x80 nt
	global_load_dwordx4 v[102:105], v[194:195], off offset:0xa0 nt
	global_load_dwordx4 v[106:109], v[194:195], off offset:0xc0 nt
	global_load_dwordx4 v[110:113], v[194:195], off offset:0xe0 nt
	global_load_dwordx4 v[114:117], v[196:197], off offset:0 nt
	global_load_dwordx4 v[118:121], v[196:197], off offset:32 nt
	global_load_dwordx4 v[122:125], v[196:197], off offset:64 nt
	global_load_dwordx4 v[126:129], v[196:197], off offset:0x60 nt
	global_load_dwordx4 v[130:133], v[196:197], off offset:0x80 nt
	global_load_dwordx4 v[134:137], v[196:197], off offset:0xa0 nt
	global_load_dwordx4 v[138:141], v[196:197], off offset:0xc0 nt
	global_load_dwordx4 v[142:145], v[196:197], off offset:0xe0 nt
	global_load_dwordx2 v[182:183], v[198:199], off nt
